# P6 projection stores marked nt (streaming)
# baseline (speedup 1.0000x reference)
.LBB0_974:
	s_nop 0
	v_cndmask_b32_e64 v4, 0, 1, s[4:5]
	v_cmp_ne_u32_e64 s[38:39], 1, v4
	v_or_b32_e32 v4, s13, v180
	v_mad_u32_u24 v228, v4, s33, v2
	ds_read_b128 v[4:7], v228
	ds_read_b128 v[196:199], v228 offset:32
	ds_read_b128 v[204:207], v228 offset:64
	ds_read_b128 v[208:211], v228 offset:96
	ds_read_b128 v[212:215], v228 offset:128
	ds_read_b128 v[216:219], v228 offset:160
	ds_read_b128 v[220:223], v228 offset:192
	ds_read_b128 v[224:227], v228 offset:224
	s_waitcnt lgkmcnt(7)
	v_mfma_f32_32x32x16_bf16 v[20:35], v[36:39], v[4:7], 0
	v_mfma_f32_32x32x16_bf16 v[4:19], v[100:103], v[4:7], 0
	s_waitcnt lgkmcnt(6)
	v_mfma_f32_32x32x16_bf16 v[20:35], v[40:43], v[196:199], v[20:35]
	v_mfma_f32_32x32x16_bf16 v[4:19], v[104:107], v[196:199], v[4:19]
	s_waitcnt lgkmcnt(5)
	v_mfma_f32_32x32x16_bf16 v[20:35], v[44:47], v[204:207], v[20:35]
	v_mfma_f32_32x32x16_bf16 v[4:19], v[108:111], v[204:207], v[4:19]
	s_waitcnt lgkmcnt(4)
	v_mfma_f32_32x32x16_bf16 v[20:35], v[48:51], v[208:211], v[20:35]
	v_mfma_f32_32x32x16_bf16 v[4:19], v[112:115], v[208:211], v[4:19]
	s_waitcnt lgkmcnt(3)
	v_mfma_f32_32x32x16_bf16 v[20:35], v[52:55], v[212:215], v[20:35]
	v_mfma_f32_32x32x16_bf16 v[4:19], v[116:119], v[212:215], v[4:19]
	s_waitcnt lgkmcnt(2)
	v_mfma_f32_32x32x16_bf16 v[20:35], v[56:59], v[216:219], v[20:35]
	v_mfma_f32_32x32x16_bf16 v[4:19], v[120:123], v[216:219], v[4:19]
	s_waitcnt lgkmcnt(1)
	v_mfma_f32_32x32x16_bf16 v[20:35], v[60:63], v[220:223], v[20:35]
	v_mfma_f32_32x32x16_bf16 v[4:19], v[124:127], v[220:223], v[4:19]
	s_waitcnt lgkmcnt(0)
	v_mfma_f32_32x32x16_bf16 v[20:35], v[64:67], v[224:227], v[20:35]
	v_mfma_f32_32x32x16_bf16 v[4:19], v[128:131], v[224:227], v[4:19]
	ds_read_b128 v[196:199], v228 offset:256
	ds_read_b128 v[204:207], v228 offset:288
	ds_read_b128 v[208:211], v228 offset:320
	ds_read_b128 v[212:215], v228 offset:352
	ds_read_b128 v[216:219], v228 offset:384
	ds_read_b128 v[220:223], v228 offset:416
	ds_read_b128 v[224:227], v228 offset:448
	ds_read_b128 v[228:231], v228 offset:480
	s_waitcnt lgkmcnt(7)
	v_mfma_f32_32x32x16_bf16 v[20:35], v[68:71], v[196:199], v[20:35]
	s_mov_b64 s[4:5], 0
	v_mfma_f32_32x32x16_bf16 v[4:19], v[132:135], v[196:199], v[4:19]
	v_or_b32_e32 v196, s13, v194
	v_mov_b32_e32 v197, v195
	s_mov_b32 s13, 32
	s_waitcnt lgkmcnt(6)
	v_mfma_f32_32x32x16_bf16 v[20:35], v[72:75], v[204:207], v[20:35]
	v_mfma_f32_32x32x16_bf16 v[4:19], v[136:139], v[204:207], v[4:19]
	s_waitcnt lgkmcnt(5)
	v_mfma_f32_32x32x16_bf16 v[20:35], v[76:79], v[208:211], v[20:35]
	v_mfma_f32_32x32x16_bf16 v[4:19], v[140:143], v[208:211], v[4:19]
	s_waitcnt lgkmcnt(4)
	v_mfma_f32_32x32x16_bf16 v[20:35], v[80:83], v[212:215], v[20:35]
	v_mfma_f32_32x32x16_bf16 v[4:19], v[144:147], v[212:215], v[4:19]
	s_waitcnt lgkmcnt(3)
	v_mfma_f32_32x32x16_bf16 v[20:35], v[84:87], v[216:219], v[20:35]
	v_mfma_f32_32x32x16_bf16 v[4:19], v[148:151], v[216:219], v[4:19]
	s_waitcnt lgkmcnt(2)
	v_mfma_f32_32x32x16_bf16 v[20:35], v[88:91], v[220:223], v[20:35]
	v_mfma_f32_32x32x16_bf16 v[4:19], v[152:155], v[220:223], v[4:19]
	s_waitcnt lgkmcnt(1)
	v_mfma_f32_32x32x16_bf16 v[20:35], v[92:95], v[224:227], v[20:35]
	v_mfma_f32_32x32x16_bf16 v[4:19], v[160:163], v[224:227], v[4:19]
	s_waitcnt lgkmcnt(0)
	v_mfma_f32_32x32x16_bf16 v[20:35], v[96:99], v[228:231], v[20:35]
	v_mfma_f32_32x32x16_bf16 v[4:19], v[164:167], v[228:231], v[4:19]
	s_nop 10
	v_cvt_pk_bf16_f32 v20, v20, v21
	v_cvt_pk_bf16_f32 v21, v22, v23
	v_cvt_pk_bf16_f32 v22, v24, v25
	v_lshl_add_u64 v[24:25], v[196:197], 4, v[188:189]
	v_cvt_pk_bf16_f32 v23, v26, v27
	v_permlane32_swap_b32_e32 v20, v22
	v_cvt_pk_bf16_f32 v4, v4, v5
	v_cvt_pk_bf16_f32 v5, v6, v7
	v_cvt_pk_bf16_f32 v6, v8, v9
	v_cvt_pk_bf16_f32 v7, v10, v11
	v_add_co_u32_e32 v8, vcc, s25, v24
	v_permlane32_swap_b32_e32 v21, v23
	v_permlane32_swap_b32_e32 v4, v6
	v_permlane32_swap_b32_e32 v5, v7
	v_addc_co_u32_e32 v9, vcc, 0, v25, vcc
	global_store_dwordx4 v[24:25], v[20:23], off nt
	global_store_dwordx4 v[8:9], v[4:7], off nt
	s_and_b64 vcc, exec, s[38:39]
	v_cvt_pk_bf16_f32 v20, v28, v29
	v_cvt_pk_bf16_f32 v21, v30, v31
	v_cvt_pk_bf16_f32 v22, v32, v33
	v_cvt_pk_bf16_f32 v23, v34, v35
	v_cvt_pk_bf16_f32 v4, v12, v13
	v_cvt_pk_bf16_f32 v5, v14, v15
	v_cvt_pk_bf16_f32 v6, v16, v17
	v_cvt_pk_bf16_f32 v7, v18, v19
	v_permlane32_swap_b32_e32 v20, v22
	v_permlane32_swap_b32_e32 v21, v23
	v_permlane32_swap_b32_e32 v4, v6
	v_permlane32_swap_b32_e32 v5, v7
	global_store_dwordx4 v[24:25], v[20:23], off offset:2048 nt
	global_store_dwordx4 v[8:9], v[4:7], off offset:2048 nt
	s_cbranch_vccz .LBB0_974
	s_xor_b32 s9, s9, 1
	s_and_b64 vcc, exec, s[14:15]
	s_cbranch_vccz .LBB0_970
	s_mul_i32 s4, s9, 0x8400
	v_add_u32_e32 v2, s4, v181
	s_waitcnt vmcnt(11)
	ds_write_b128 v2, v[156:159]
	s_waitcnt vmcnt(10)
	ds_write_b128 v2, v[168:171] offset:8448
	s_waitcnt vmcnt(9)
	ds_write_b128 v2, v[172:175] offset:16896
	s_waitcnt vmcnt(8)
	ds_write_b128 v2, v[176:179] offset:25344
	s_branch .LBB0_970
